# stack12 + first super-phase fragment ds_reads issued at the top of the unit header (7 GEMM phases) so LDS latency overlaps the scalar unit decode
# baseline (speedup 1.0000x reference)
.LBB0_159:
	v_readlane_b32 s30, v254, 1
	v_readlane_b32 s31, v254, 2
	s_mov_b32 s15, s99
	s_add_i32 s63, s63, 1
	s_mul_i32 s12, s63, s54
	s_waitcnt lgkmcnt(0)
	ds_read_b128 v[90:93], v197
	ds_read_b128 v[94:97], v197 offset:1024
	ds_read_b128 v[98:101], v197 offset:2048
	ds_read_b128 v[102:105], v197 offset:3072
	ds_read_b128 v[146:149], v198
	ds_read_b128 v[150:153], v198 offset:1024
	ds_read_b128 v[180:183], v198 offset:2048
	ds_read_b128 v[184:187], v198 offset:3072
	ds_read_b128 v[188:191], v199
	ds_read_b128 v[192:195], v199 offset:1024
	ds_read_b128 v[200:203], v199 offset:2048
	ds_read_b128 v[204:207], v199 offset:3072
	ds_read_b128 v[208:211], v199 offset:4096
	ds_read_b128 v[216:219], v199 offset:5120
	ds_read_b128 v[220:223], v199 offset:6144
	ds_read_b128 v[224:227], v199 offset:7168
	s_mul_hi_u32 s13, s63, s15
	s_add_i32 s13, s13, s12
	s_mul_i32 s12, s63, s15
	v_readlane_b32 s15, v254, 14
	s_add_u32 s30, s12, s15
	s_addc_u32 s31, s13, s55
	v_cmp_gt_i64_e32 vcc, s[30:31], v[178:179]
	v_cmp_lt_i64_e64 s[12:13], s[30:31], v[176:177]
	s_cbranch_vccnz .LBB0_161
	s_ashr_i32 s15, s30, 31
	s_lshr_b32 s15, s15, 29
	s_add_i32 s15, s30, s15
	s_ashr_i32 s26, s15, 3
	s_and_b32 s15, s15, -8
	s_sub_i32 s15, s30, s15
	s_cmp_lt_i32 s15, 0
	s_cselect_b32 s27, s56, 0x140
	s_mul_i32 s15, s15, s27
	s_add_i32 s15, s15, s26
	s_mul_hi_i32 s26, s15, 0x66666667
	s_lshr_b32 s27, s26, 31
	s_ashr_i32 s26, s26, 6
	s_add_i32 s26, s26, s27
	s_lshl_b32 s27, s26, 3
	s_sub_i32 s28, 0x80, s27
	s_min_i32 s28, s28, 8
	s_abs_i32 s29, s28
	v_cvt_f32_u32_e32 v2, s29
	s_sub_i32 s31, 0, s29
	s_mulk_i32 s26, 0xa0
	s_sub_i32 s15, s15, s26
	v_rcp_iflag_f32_e32 v2, v2
	s_abs_i32 s26, s15
	s_xor_b32 s30, s15, s28
	s_ashr_i32 s30, s30, 31
	v_mul_f32_e32 v2, 0x4f7ffffe, v2
	v_cvt_u32_f32_e32 v2, v2
	s_nop 0
	v_readfirstlane_b32 s34, v2
	s_mul_i32 s31, s31, s34
	s_mul_hi_u32 s31, s34, s31
	s_add_i32 s34, s34, s31
	s_mul_hi_u32 s31, s26, s34
	s_mul_i32 s34, s31, s29
	s_sub_i32 s26, s26, s34
	s_add_i32 s35, s31, 1
	s_sub_i32 s34, s26, s29
	s_cmp_ge_u32 s26, s29
	s_cselect_b32 s31, s35, s31
	s_cselect_b32 s26, s34, s26
	s_add_i32 s34, s31, 1
	s_cmp_ge_u32 s26, s29
	s_cselect_b32 s26, s34, s31
	s_xor_b32 s26, s26, s30
	s_sub_i32 s26, s26, s30
	s_mul_i32 s28, s26, s28
	s_sub_i32 s15, s15, s28
	s_add_i32 s28, s27, s15
.LBB0_161:
	s_ashr_i32 s29, s28, 31
	s_lshl_b64 s[30:31], s[28:29], 20
	v_readlane_b32 s34, v254, 18
	v_readlane_b32 s35, v254, 19
	s_add_u32 s30, s34, s30
	s_addc_u32 s31, s35, s31
	s_and_b64 s[34:35], s[12:13], exec
	s_cselect_b32 s15, s31, s17
	s_cselect_b32 s29, s30, s16
	s_ashr_i32 s27, s26, 31
	s_lshl_b64 s[34:35], s[26:27], 20
	s_add_u32 s34, s33, s34
	s_addc_u32 s35, s42, s35
	s_and_b64 s[38:39], s[12:13], exec
	s_cselect_b32 s27, s35, s37
	s_cselect_b32 s40, s34, s36
	s_add_u32 s16, s16, 0x80080
	s_addc_u32 s17, s17, 0
	s_add_u32 s41, s36, 0x100
	s_addc_u32 s64, s37, 0
	s_mov_b32 s65, -2
	s_add_u32 s36, s16, 0xfff80080
	s_addc_u32 s37, s17, -1
	s_cmp_eq_u32 s65, 28
	s_cselect_b32 s39, s15, s37
	s_cselect_b32 s38, s29, s36
	s_cselect_b32 s37, s27, s64
	s_cselect_b32 s36, s40, s41
	v_lshl_add_u64 v[212:213], s[16:17], 0, v[172:173]
	s_add_i32 m0, s44, 0xc000
	global_load_lds_dwordx4 v[212:213], off
	v_lshl_add_u64 v[212:213], s[16:17], 0, v[174:175]
	s_add_i32 m0, s44, 0xe000
	s_nop 0
	global_load_lds_dwordx4 v[212:213], off
	s_waitcnt vmcnt(8)
	s_waitcnt lgkmcnt(0)
	s_setprio 1
	s_barrier
	v_mfma_f32_16x16x32_bf16 v[70:73], v[90:93], v[188:191], 0
	v_mfma_f32_16x16x32_bf16 v[66:69], v[98:101], v[188:191], 0
	v_mfma_f32_16x16x32_bf16 v[54:57], v[90:93], v[200:203], 0
	v_mfma_f32_16x16x32_bf16 v[50:53], v[98:101], v[200:203], 0
	v_mfma_f32_16x16x32_bf16 v[46:49], v[90:93], v[208:211], 0
	v_mfma_f32_16x16x32_bf16 v[42:45], v[98:101], v[208:211], 0
	v_mfma_f32_16x16x32_bf16 v[38:41], v[90:93], v[220:223], 0
	v_mfma_f32_16x16x32_bf16 v[34:37], v[98:101], v[220:223], 0
	v_mfma_f32_16x16x32_bf16 v[70:73], v[94:97], v[192:195], v[70:73]
	v_mfma_f32_16x16x32_bf16 v[66:69], v[102:105], v[192:195], v[66:69]
	v_mfma_f32_16x16x32_bf16 v[54:57], v[94:97], v[204:207], v[54:57]
	v_mfma_f32_16x16x32_bf16 v[50:53], v[102:105], v[204:207], v[50:53]
	v_mfma_f32_16x16x32_bf16 v[46:49], v[94:97], v[216:219], v[46:49]
	v_mfma_f32_16x16x32_bf16 v[42:45], v[102:105], v[216:219], v[42:45]
	v_mfma_f32_16x16x32_bf16 v[38:41], v[94:97], v[224:227], v[38:41]
	v_mfma_f32_16x16x32_bf16 v[34:37], v[102:105], v[224:227], v[34:37]
	s_setprio 0
	s_setprio 1
	v_mfma_f32_16x16x32_bf16 v[142:145], v[146:149], v[188:191], 0
	v_mfma_f32_16x16x32_bf16 v[138:141], v[180:183], v[188:191], 0
	v_mfma_f32_16x16x32_bf16 v[134:137], v[146:149], v[200:203], 0
	v_mfma_f32_16x16x32_bf16 v[130:133], v[180:183], v[200:203], 0
	v_mfma_f32_16x16x32_bf16 v[126:129], v[146:149], v[208:211], 0
	v_mfma_f32_16x16x32_bf16 v[122:125], v[180:183], v[208:211], 0
	v_mfma_f32_16x16x32_bf16 v[118:121], v[146:149], v[220:223], 0
	v_mfma_f32_16x16x32_bf16 v[114:117], v[180:183], v[220:223], 0
	v_mfma_f32_16x16x32_bf16 v[142:145], v[150:153], v[192:195], v[142:145]
	v_mfma_f32_16x16x32_bf16 v[138:141], v[184:187], v[192:195], v[138:141]
	v_mfma_f32_16x16x32_bf16 v[134:137], v[150:153], v[204:207], v[134:137]
	v_mfma_f32_16x16x32_bf16 v[130:133], v[184:187], v[204:207], v[130:133]
	v_mfma_f32_16x16x32_bf16 v[126:129], v[150:153], v[216:219], v[126:129]
	v_mfma_f32_16x16x32_bf16 v[122:125], v[184:187], v[216:219], v[122:125]
	v_mfma_f32_16x16x32_bf16 v[118:121], v[150:153], v[224:227], v[118:121]
	v_mfma_f32_16x16x32_bf16 v[114:117], v[184:187], v[224:227], v[114:117]
	s_barrier
	s_setprio 0
	s_add_i32 s66, s57, s43
	v_lshl_add_u64 v[212:213], s[36:37], 0, v[156:157]
	s_mov_b32 m0, s66
	ds_read_b128 v[188:191], v199 offset:16384
	ds_read_b128 v[192:195], v199 offset:17408
	ds_read_b128 v[200:203], v199 offset:18432
	ds_read_b128 v[204:207], v199 offset:19456
	ds_read_b128 v[208:211], v199 offset:20480
	ds_read_b128 v[216:219], v199 offset:21504
	ds_read_b128 v[220:223], v199 offset:22528
	ds_read_b128 v[224:227], v199 offset:23552
	global_load_lds_dwordx4 v[212:213], off
	s_add_i32 m0, s66, 0x2000
	s_add_u32 s66, s36, 0x80000
	v_lshl_add_u64 v[214:215], s[36:37], 0, v[160:161]
	s_addc_u32 s67, s37, 0
	s_add_i32 s68, s58, s43
	global_load_lds_dwordx4 v[214:215], off
	v_lshl_add_u64 v[228:229], s[66:67], 0, v[156:157]
	s_mov_b32 m0, s68
	v_lshl_add_u64 v[230:231], s[38:39], 0, v[158:159]
	global_load_lds_dwordx4 v[228:229], off
	v_lshl_add_u64 v[228:229], s[66:67], 0, v[160:161]
	s_add_i32 m0, s68, 0x2000
	s_nop 0
	global_load_lds_dwordx4 v[228:229], off
	v_lshl_add_u64 v[228:229], s[38:39], 0, v[154:155]
	s_mov_b32 m0, s44
	s_nop 0
	global_load_lds_dwordx4 v[228:229], off
	s_mov_b32 m0, s45
	s_nop 0
	global_load_lds_dwordx4 v[230:231], off
	s_waitcnt vmcnt(8)
	s_waitcnt lgkmcnt(0)
	s_setprio 1
	s_barrier
	v_mfma_f32_16x16x32_bf16 v[30:33], v[90:93], v[188:191], 0
	v_mfma_f32_16x16x32_bf16 v[26:29], v[98:101], v[188:191], 0
	v_mfma_f32_16x16x32_bf16 v[22:25], v[90:93], v[200:203], 0
	v_mfma_f32_16x16x32_bf16 v[18:21], v[98:101], v[200:203], 0
	v_mfma_f32_16x16x32_bf16 v[14:17], v[90:93], v[208:211], 0
	v_mfma_f32_16x16x32_bf16 v[10:13], v[98:101], v[208:211], 0
	v_mfma_f32_16x16x32_bf16 v[6:9], v[90:93], v[220:223], 0
	v_mfma_f32_16x16x32_bf16 v[2:5], v[98:101], v[220:223], 0
	v_mfma_f32_16x16x32_bf16 v[30:33], v[94:97], v[192:195], v[30:33]
	v_mfma_f32_16x16x32_bf16 v[26:29], v[102:105], v[192:195], v[26:29]
	v_mfma_f32_16x16x32_bf16 v[22:25], v[94:97], v[204:207], v[22:25]
	v_mfma_f32_16x16x32_bf16 v[18:21], v[102:105], v[204:207], v[18:21]
	v_mfma_f32_16x16x32_bf16 v[14:17], v[94:97], v[216:219], v[14:17]
	v_mfma_f32_16x16x32_bf16 v[10:13], v[102:105], v[216:219], v[10:13]
	v_mfma_f32_16x16x32_bf16 v[6:9], v[94:97], v[224:227], v[6:9]
	v_mfma_f32_16x16x32_bf16 v[2:5], v[102:105], v[224:227], v[2:5]
	s_setprio 0
	s_setprio 1
	v_mfma_f32_16x16x32_bf16 v[86:89], v[146:149], v[200:203], 0
	v_mfma_f32_16x16x32_bf16 v[82:85], v[180:183], v[200:203], 0
	v_mfma_f32_16x16x32_bf16 v[78:81], v[146:149], v[208:211], 0
	v_mfma_f32_16x16x32_bf16 v[74:77], v[180:183], v[208:211], 0
	v_mfma_f32_16x16x32_bf16 v[62:65], v[146:149], v[220:223], 0
	v_mfma_f32_16x16x32_bf16 v[58:61], v[180:183], v[220:223], 0
	v_mfma_f32_16x16x32_bf16 v[90:93], v[146:149], v[188:191], 0
	v_mfma_f32_16x16x32_bf16 v[94:97], v[180:183], v[188:191], 0
	v_mfma_f32_16x16x32_bf16 v[86:89], v[150:153], v[204:207], v[86:89]
	v_mfma_f32_16x16x32_bf16 v[82:85], v[184:187], v[204:207], v[82:85]
	v_mfma_f32_16x16x32_bf16 v[78:81], v[150:153], v[216:219], v[78:81]
	v_mfma_f32_16x16x32_bf16 v[74:77], v[184:187], v[216:219], v[74:77]
	v_mfma_f32_16x16x32_bf16 v[62:65], v[150:153], v[224:227], v[62:65]
	v_mfma_f32_16x16x32_bf16 v[58:61], v[184:187], v[224:227], v[58:61]
	v_mfma_f32_16x16x32_bf16 v[90:93], v[150:153], v[192:195], v[90:93]
	v_mfma_f32_16x16x32_bf16 v[94:97], v[184:187], v[192:195], v[94:97]
	s_barrier
	s_setprio 0
	s_add_i32 s66, 0, 0x18000
	s_add_i32 s67, 0, 0x1c000
	v_add_u32_e32 v110, s66, v165
	v_add_u32_e32 v162, s67, v165
	ds_read_b128 v[98:101], v110
	ds_read_b128 v[102:105], v110 offset:1024
	ds_read_b128 v[106:109], v110 offset:2048
	ds_read_b128 v[110:113], v110 offset:3072
	ds_read_b128 v[146:149], v162
	ds_read_b128 v[150:153], v162 offset:1024
	ds_read_b128 v[180:183], v162 offset:2048
	ds_read_b128 v[184:187], v162 offset:3072
	s_add_u32 s38, s38, 0x80000
	s_addc_u32 s39, s39, 0
	s_mov_b32 m0, s47
	v_lshl_add_u64 v[232:233], s[38:39], 0, v[154:155]
	ds_read_b128 v[188:191], v199 offset:32768
	ds_read_b128 v[192:195], v199 offset:33792
	ds_read_b128 v[200:203], v199 offset:34816
	ds_read_b128 v[204:207], v199 offset:35840
	ds_read_b128 v[208:211], v199 offset:36864
	ds_read_b128 v[216:219], v199 offset:37888
	ds_read_b128 v[220:223], v199 offset:38912
	ds_read_b128 v[224:227], v199 offset:39936
	global_load_lds_dwordx4 v[232:233], off
	v_lshl_add_u64 v[232:233], s[38:39], 0, v[158:159]
	s_mov_b32 m0, s48
	s_nop 0
	global_load_lds_dwordx4 v[232:233], off
	s_waitcnt vmcnt(8)
	s_waitcnt lgkmcnt(0)
	s_setprio 1
	s_barrier
	v_mfma_f32_16x16x32_bf16 v[70:73], v[98:101], v[188:191], v[70:73]
	v_mfma_f32_16x16x32_bf16 v[66:69], v[106:109], v[188:191], v[66:69]
	v_mfma_f32_16x16x32_bf16 v[54:57], v[98:101], v[200:203], v[54:57]
	v_mfma_f32_16x16x32_bf16 v[50:53], v[106:109], v[200:203], v[50:53]
	v_mfma_f32_16x16x32_bf16 v[46:49], v[98:101], v[208:211], v[46:49]
	v_mfma_f32_16x16x32_bf16 v[42:45], v[106:109], v[208:211], v[42:45]
	v_mfma_f32_16x16x32_bf16 v[38:41], v[98:101], v[220:223], v[38:41]
	v_mfma_f32_16x16x32_bf16 v[34:37], v[106:109], v[220:223], v[34:37]
	v_mfma_f32_16x16x32_bf16 v[70:73], v[102:105], v[192:195], v[70:73]
	v_mfma_f32_16x16x32_bf16 v[66:69], v[110:113], v[192:195], v[66:69]
	v_mfma_f32_16x16x32_bf16 v[54:57], v[102:105], v[204:207], v[54:57]
	v_mfma_f32_16x16x32_bf16 v[50:53], v[110:113], v[204:207], v[50:53]
	v_mfma_f32_16x16x32_bf16 v[46:49], v[102:105], v[216:219], v[46:49]
	v_mfma_f32_16x16x32_bf16 v[42:45], v[110:113], v[216:219], v[42:45]
	v_mfma_f32_16x16x32_bf16 v[38:41], v[102:105], v[224:227], v[38:41]
	v_mfma_f32_16x16x32_bf16 v[34:37], v[110:113], v[224:227], v[34:37]
	s_setprio 0
	s_setprio 1
	v_mfma_f32_16x16x32_bf16 v[142:145], v[146:149], v[188:191], v[142:145]
	v_mfma_f32_16x16x32_bf16 v[138:141], v[180:183], v[188:191], v[138:141]
	v_mfma_f32_16x16x32_bf16 v[134:137], v[146:149], v[200:203], v[134:137]
	v_mfma_f32_16x16x32_bf16 v[130:133], v[180:183], v[200:203], v[130:133]
	v_mfma_f32_16x16x32_bf16 v[126:129], v[146:149], v[208:211], v[126:129]
	v_mfma_f32_16x16x32_bf16 v[122:125], v[180:183], v[208:211], v[122:125]
	v_mfma_f32_16x16x32_bf16 v[118:121], v[146:149], v[220:223], v[118:121]
	v_mfma_f32_16x16x32_bf16 v[114:117], v[180:183], v[220:223], v[114:117]
	v_mfma_f32_16x16x32_bf16 v[142:145], v[150:153], v[192:195], v[142:145]
	v_mfma_f32_16x16x32_bf16 v[138:141], v[184:187], v[192:195], v[138:141]
	v_mfma_f32_16x16x32_bf16 v[134:137], v[150:153], v[204:207], v[134:137]
	v_mfma_f32_16x16x32_bf16 v[130:133], v[184:187], v[204:207], v[130:133]
	v_mfma_f32_16x16x32_bf16 v[126:129], v[150:153], v[216:219], v[126:129]
	v_mfma_f32_16x16x32_bf16 v[122:125], v[184:187], v[216:219], v[122:125]
	v_mfma_f32_16x16x32_bf16 v[118:121], v[150:153], v[224:227], v[118:121]
	v_mfma_f32_16x16x32_bf16 v[114:117], v[184:187], v[224:227], v[114:117]
	s_barrier
	s_setprio 0
	s_add_i32 s38, s66, s43
	v_lshl_add_u64 v[212:213], v[212:213], 0, s[18:19]
	s_mov_b32 m0, s38
	ds_read_b128 v[188:191], v199 offset:49152
	ds_read_b128 v[192:195], v199 offset:50176
	ds_read_b128 v[200:203], v199 offset:51200
	ds_read_b128 v[204:207], v199 offset:52224
	ds_read_b128 v[208:211], v199 offset:53248
	ds_read_b128 v[216:219], v199 offset:54272
	ds_read_b128 v[220:223], v199 offset:55296
	ds_read_b128 v[224:227], v199 offset:56320
	global_load_lds_dwordx4 v[212:213], off
	s_add_i32 m0, s38, 0x2000
	s_add_u32 s36, s36, 0x80080
	v_lshl_add_u64 v[212:213], v[214:215], 0, s[18:19]
	s_addc_u32 s37, s37, 0
	s_add_i32 s38, s67, s43
	global_load_lds_dwordx4 v[212:213], off
	v_lshl_add_u64 v[212:213], s[36:37], 0, v[156:157]
	s_mov_b32 m0, s38
	s_nop 0
	global_load_lds_dwordx4 v[212:213], off
	v_lshl_add_u64 v[212:213], s[36:37], 0, v[160:161]
	s_add_i32 m0, s38, 0x2000
	s_nop 0
	global_load_lds_dwordx4 v[212:213], off
	v_lshl_add_u64 v[212:213], v[228:229], 0, s[18:19]
	s_mov_b32 m0, s52
	s_nop 0
	global_load_lds_dwordx4 v[212:213], off
	v_lshl_add_u64 v[212:213], v[230:231], 0, s[18:19]
	s_mov_b32 m0, s53
	s_nop 0
	global_load_lds_dwordx4 v[212:213], off
	s_waitcnt vmcnt(8)
	s_waitcnt lgkmcnt(0)
	s_setprio 1
	s_barrier
	v_mfma_f32_16x16x32_bf16 v[30:33], v[98:101], v[188:191], v[30:33]
	v_mfma_f32_16x16x32_bf16 v[26:29], v[106:109], v[188:191], v[26:29]
	v_mfma_f32_16x16x32_bf16 v[22:25], v[98:101], v[200:203], v[22:25]
	v_mfma_f32_16x16x32_bf16 v[18:21], v[106:109], v[200:203], v[18:21]
	v_mfma_f32_16x16x32_bf16 v[14:17], v[98:101], v[208:211], v[14:17]
	v_mfma_f32_16x16x32_bf16 v[10:13], v[106:109], v[208:211], v[10:13]
	v_mfma_f32_16x16x32_bf16 v[6:9], v[98:101], v[220:223], v[6:9]
	v_mfma_f32_16x16x32_bf16 v[2:5], v[106:109], v[220:223], v[2:5]
	v_mfma_f32_16x16x32_bf16 v[30:33], v[102:105], v[192:195], v[30:33]
	v_mfma_f32_16x16x32_bf16 v[26:29], v[110:113], v[192:195], v[26:29]
	v_mfma_f32_16x16x32_bf16 v[22:25], v[102:105], v[204:207], v[22:25]
	v_mfma_f32_16x16x32_bf16 v[18:21], v[110:113], v[204:207], v[18:21]
	v_mfma_f32_16x16x32_bf16 v[14:17], v[102:105], v[216:219], v[14:17]
	v_mfma_f32_16x16x32_bf16 v[10:13], v[110:113], v[216:219], v[10:13]
	v_mfma_f32_16x16x32_bf16 v[6:9], v[102:105], v[224:227], v[6:9]
	v_mfma_f32_16x16x32_bf16 v[2:5], v[110:113], v[224:227], v[2:5]
	s_setprio 0
	s_setprio 1
	v_mfma_f32_16x16x32_bf16 v[90:93], v[146:149], v[188:191], v[90:93]
	v_mfma_f32_16x16x32_bf16 v[110:113], v[150:153], v[192:195], v[90:93]
	v_mfma_f32_16x16x32_bf16 v[90:93], v[180:183], v[188:191], v[94:97]
	v_mfma_f32_16x16x32_bf16 v[86:89], v[146:149], v[200:203], v[86:89]
	v_mfma_f32_16x16x32_bf16 v[82:85], v[180:183], v[200:203], v[82:85]
	v_mfma_f32_16x16x32_bf16 v[78:81], v[146:149], v[208:211], v[78:81]
	v_mfma_f32_16x16x32_bf16 v[74:77], v[180:183], v[208:211], v[74:77]
	v_mfma_f32_16x16x32_bf16 v[62:65], v[146:149], v[220:223], v[62:65]
	v_mfma_f32_16x16x32_bf16 v[58:61], v[180:183], v[220:223], v[58:61]
	v_mfma_f32_16x16x32_bf16 v[106:109], v[184:187], v[192:195], v[90:93]
	v_mfma_f32_16x16x32_bf16 v[86:89], v[150:153], v[204:207], v[86:89]
	v_mfma_f32_16x16x32_bf16 v[82:85], v[184:187], v[204:207], v[82:85]
	v_mfma_f32_16x16x32_bf16 v[78:81], v[150:153], v[216:219], v[78:81]
	v_mfma_f32_16x16x32_bf16 v[74:77], v[184:187], v[216:219], v[74:77]
	v_mfma_f32_16x16x32_bf16 v[62:65], v[150:153], v[224:227], v[62:65]
	v_mfma_f32_16x16x32_bf16 v[58:61], v[184:187], v[224:227], v[58:61]
	s_barrier
	s_setprio 0
	s_add_i32 s65, s65, 2
	s_add_u32 s16, s16, 0x100
	s_addc_u32 s17, s17, 0
	s_add_u32 s41, s41, 0x100
	s_addc_u32 s64, s64, 0
	s_cmp_gt_u32 s65, 29

.LBB0_1339:
	v_readlane_b32 s24, v254, 1
	v_readlane_b32 s25, v254, 2
	s_mov_b32 s21, s99
	s_add_i32 s44, s44, 1
	s_mul_i32 s8, s44, s47
	s_waitcnt lgkmcnt(0)
	ds_read_b128 v[154:157], v150
	ds_read_b128 v[158:161], v150 offset:1024
	ds_read_b128 v[162:165], v150 offset:2048
	ds_read_b128 v[166:169], v150 offset:3072
	ds_read_b128 v[170:173], v151
	ds_read_b128 v[174:177], v151 offset:1024
	ds_read_b128 v[178:181], v151 offset:2048
	ds_read_b128 v[182:185], v151 offset:3072
	ds_read_b128 v[186:189], v152
	ds_read_b128 v[190:193], v152 offset:1024
	ds_read_b128 v[194:197], v152 offset:2048
	ds_read_b128 v[198:201], v152 offset:3072
	ds_read_b128 v[202:205], v152 offset:4096
	ds_read_b128 v[206:209], v152 offset:5120
	ds_read_b128 v[210:213], v152 offset:6144
	ds_read_b128 v[214:217], v152 offset:7168
	s_mul_hi_u32 s9, s44, s21
	s_add_i32 s9, s9, s8
	s_mul_i32 s8, s44, s21
	v_readlane_b32 s21, v254, 14
	s_add_u32 s24, s8, s21
	s_addc_u32 s25, s9, s33
	v_cmp_gt_i64_e32 vcc, s[24:25], v[144:145]
	v_cmp_lt_i64_e64 s[8:9], s[24:25], v[142:143]
	s_cbranch_vccnz .LBB0_1345
	s_ashr_i32 s20, s24, 31
	s_lshr_b32 s20, s20, 29
	s_add_i32 s22, s24, s20
	s_and_b32 s20, s22, -8
	s_sub_i32 s23, s24, s20
	s_cmp_gt_i32 s23, -1
	s_mov_b64 s[20:21], -1
	s_cbranch_scc0 .LBB0_1342
	s_lshl_b32 s24, s23, 7
	s_mov_b64 s[20:21], 0

.LBB0_1345:
	s_ashr_i32 s23, s22, 31
	s_lshl_b64 s[24:25], s[22:23], 20
	v_readlane_b32 s26, v254, 22
	v_readlane_b32 s27, v254, 23
	s_add_u32 s24, s26, s24
	s_addc_u32 s25, s27, s25
	s_and_b64 s[26:27], s[8:9], exec
	s_cselect_b32 s23, s25, s31
	s_cselect_b32 s55, s24, s30
	s_ashr_i32 s21, s20, 31
	s_lshl_b64 s[26:27], s[20:21], 20
	s_add_u32 s26, s38, s26
	s_addc_u32 s27, s39, s27
	s_and_b64 s[36:37], s[8:9], exec
	s_cselect_b32 s21, s27, s35
	s_cselect_b32 s56, s26, s34
	s_add_u32 s30, s30, 0x80080
	s_addc_u32 s31, s31, 0
	s_add_u32 s57, s34, 0x100
	s_addc_u32 s58, s35, 0
	s_mov_b32 s59, -2
	s_add_u32 s34, s30, 0xfff80080
	s_addc_u32 s35, s31, -1
	s_cmp_eq_u32 s59, 28
	s_cselect_b32 s37, s23, s35
	s_cselect_b32 s36, s55, s34
	s_cselect_b32 s35, s21, s58
	s_cselect_b32 s34, s56, s57
	v_lshl_add_u64 v[146:147], s[30:31], 0, v[138:139]
	s_add_i32 m0, s29, 0xc000
	global_load_lds_dwordx4 v[146:147], off
	v_lshl_add_u64 v[146:147], s[30:31], 0, v[140:141]
	s_add_i32 m0, s29, 0xe000
	s_nop 0
	global_load_lds_dwordx4 v[146:147], off
	s_cmp_lg_u32 s100, 0
	s_cbranch_scc1 .Lrx_1346_0
	s_waitcnt vmcnt(8)

.LBB0_1476:
	v_readlane_b32 s22, v254, 1
	v_readlane_b32 s23, v254, 2
	s_mov_b32 s17, s99
	s_add_i32 s43, s43, 1
	s_mul_i32 s8, s43, s46
	s_waitcnt lgkmcnt(0)
	ds_read_b128 v[154:157], v150
	ds_read_b128 v[158:161], v150 offset:1024
	ds_read_b128 v[162:165], v150 offset:2048
	ds_read_b128 v[166:169], v150 offset:3072
	ds_read_b128 v[170:173], v151
	ds_read_b128 v[174:177], v151 offset:1024
	ds_read_b128 v[178:181], v151 offset:2048
	ds_read_b128 v[182:185], v151 offset:3072
	ds_read_b128 v[186:189], v152
	ds_read_b128 v[190:193], v152 offset:1024
	ds_read_b128 v[194:197], v152 offset:2048
	ds_read_b128 v[198:201], v152 offset:3072
	ds_read_b128 v[202:205], v152 offset:4096
	ds_read_b128 v[206:209], v152 offset:5120
	ds_read_b128 v[210:213], v152 offset:6144
	ds_read_b128 v[214:217], v152 offset:7168
	s_mul_hi_u32 s9, s43, s17
	s_add_i32 s9, s9, s8
	s_mul_i32 s8, s43, s17
	v_readlane_b32 s17, v254, 14
	s_add_u32 s22, s8, s17
	s_addc_u32 s23, s9, s37
	v_cmp_gt_i64_e32 vcc, s[22:23], v[146:147]
	v_cmp_lt_i64_e64 s[8:9], s[22:23], v[144:145]
	s_cbranch_vccnz .LBB0_1478
	s_ashr_i32 s16, s22, 31
	s_lshr_b32 s16, s16, 29
	s_add_i32 s16, s22, s16
	s_ashr_i32 s17, s16, 3
	s_and_b32 s16, s16, -8
	s_sub_i32 s16, s22, s16
	s_cmp_lt_i32 s16, 0
	s_cselect_b32 s18, s38, 0x2c0
	s_mul_i32 s16, s16, s18
	s_add_i32 s16, s16, s17
	s_mul_hi_i32 s17, s16, 0x2e8ba2e9
	s_lshr_b32 s18, s17, 31
	s_ashr_i32 s17, s17, 6
	s_add_i32 s17, s17, s18
	s_lshl_b32 s18, s17, 3
	s_sub_i32 s19, 0x80, s18
	s_min_i32 s19, s19, 8
	s_abs_i32 s22, s19
	v_cvt_f32_u32_e32 v2, s22
	s_sub_i32 s24, 0, s22
	s_mulk_i32 s17, 0x160
	s_sub_i32 s17, s16, s17
	v_rcp_iflag_f32_e32 v2, v2
	s_abs_i32 s16, s17
	s_xor_b32 s23, s17, s19
	s_ashr_i32 s23, s23, 31
	v_mul_f32_e32 v2, 0x4f7ffffe, v2
	v_cvt_u32_f32_e32 v2, v2
	s_nop 0
	v_readfirstlane_b32 s25, v2
	s_mul_i32 s24, s24, s25
	s_mul_hi_u32 s24, s25, s24
	s_add_i32 s25, s25, s24
	s_mul_hi_u32 s24, s16, s25
	s_mul_i32 s25, s24, s22
	s_sub_i32 s16, s16, s25
	s_add_i32 s27, s24, 1
	s_sub_i32 s25, s16, s22
	s_cmp_ge_u32 s16, s22
	s_cselect_b32 s24, s27, s24
	s_cselect_b32 s16, s25, s16
	s_add_i32 s25, s24, 1
	s_cmp_ge_u32 s16, s22
	s_cselect_b32 s16, s25, s24
	s_xor_b32 s16, s16, s23
	s_sub_i32 s16, s16, s23
	s_mul_i32 s19, s16, s19
	s_sub_i32 s17, s17, s19
	s_add_i32 s18, s18, s17
.LBB0_1478:
	s_ashr_i32 s19, s18, 31
	s_lshl_b64 s[22:23], s[18:19], 20
	s_add_u32 s22, s20, s22
	s_addc_u32 s23, s21, s23
	s_and_b64 s[24:25], s[8:9], exec
	s_cselect_b32 s19, s23, s29
	s_cselect_b32 s27, s22, s28
	s_ashr_i32 s17, s16, 31
	s_lshl_b64 s[24:25], s[16:17], 20
	s_add_u32 s24, s15, s24
	s_addc_u32 s25, s33, s25
	s_and_b64 s[34:35], s[8:9], exec
	s_cselect_b32 s17, s25, s31
	s_cselect_b32 s51, s24, s30
	s_lshl_b32 s34, s26, 8
	s_ashr_i32 s35, s34, 31
	v_lshl_add_u64 v[238:239], s[34:35], 2, v[138:139]
	global_load_dword v240, v[238:239], off
	global_load_dword v242, v[238:239], off offset:64
	global_load_dword v244, v[238:239], off offset:128
	global_load_dword v246, v[238:239], off offset:192
	global_load_dword v248, v[238:239], off offset:512
	global_load_dword v250, v[238:239], off offset:576
	global_load_dword v252, v[238:239], off offset:640
	global_load_dword v238, v[238:239], off offset:704
	s_add_u32 s28, s28, 0x80080
	s_addc_u32 s29, s29, 0
	s_add_u32 s52, s30, 0x100
	s_addc_u32 s53, s31, 0
	s_mov_b32 s54, -2
	s_add_u32 s30, s28, 0xfff80080
	s_addc_u32 s31, s29, -1
	s_cmp_eq_u32 s54, 28
	s_cselect_b32 s35, s19, s31
	s_cselect_b32 s34, s27, s30
	s_cselect_b32 s31, s17, s53
	s_cselect_b32 s30, s51, s52
	v_lshl_add_u64 v[218:219], s[28:29], 0, v[140:141]
	s_add_i32 m0, s39, 0xc000
	global_load_lds_dwordx4 v[218:219], off
	v_lshl_add_u64 v[218:219], s[28:29], 0, v[142:143]
	s_add_i32 m0, s39, 0xe000
	s_nop 0
	global_load_lds_dwordx4 v[218:219], off
	s_cmp_lg_u32 s100, 0
	s_cbranch_scc1 .Lrx_1479_0
	s_waitcnt vmcnt(8)

.LBB0_1551:
	v_readlane_b32 s8, v254, 1
	v_readlane_b32 s9, v254, 2
	s_mov_b32 s8, s99
	s_add_i32 s43, s43, 1
	s_mul_i32 s0, s43, s46
	s_waitcnt lgkmcnt(0)
	ds_read_b128 v[154:157], v150
	ds_read_b128 v[158:161], v150 offset:1024
	ds_read_b128 v[162:165], v150 offset:2048
	ds_read_b128 v[166:169], v150 offset:3072
	ds_read_b128 v[170:173], v151
	ds_read_b128 v[174:177], v151 offset:1024
	ds_read_b128 v[178:181], v151 offset:2048
	ds_read_b128 v[182:185], v151 offset:3072
	ds_read_b128 v[186:189], v152
	ds_read_b128 v[190:193], v152 offset:1024
	ds_read_b128 v[194:197], v152 offset:2048
	ds_read_b128 v[198:201], v152 offset:3072
	ds_read_b128 v[202:205], v152 offset:4096
	ds_read_b128 v[206:209], v152 offset:5120
	ds_read_b128 v[210:213], v152 offset:6144
	ds_read_b128 v[214:217], v152 offset:7168
	s_mul_hi_u32 s1, s43, s8
	s_add_i32 s1, s1, s0
	s_mul_i32 s0, s43, s8
	v_readlane_b32 s8, v254, 14
	s_add_u32 s8, s0, s8
	s_addc_u32 s9, s1, s33
	v_cmp_gt_i64_e32 vcc, s[8:9], v[144:145]
	v_cmp_lt_i64_e64 s[0:1], s[8:9], v[142:143]
	s_cbranch_vccnz .LBB0_1557
	s_ashr_i32 s9, s8, 31
	s_lshr_b32 s9, s9, 29
	s_add_i32 s24, s8, s9
	s_and_b32 s9, s24, -8
	s_sub_i32 s25, s8, s9
	s_cmp_gt_i32 s25, -1
	s_mov_b64 s[8:9], -1
	s_cbranch_scc0 .LBB0_1554
	s_lshl_b32 s30, s25, 7
	s_mov_b64 s[8:9], 0

.LBB0_1561:
	s_add_u32 s26, s26, 0x160080
	s_addc_u32 s27, s27, 0
	s_add_u32 s57, s28, 0x100
	s_addc_u32 s58, s29, 0
	s_mov_b32 s59, -2
	s_add_u32 s28, s26, 0xffea0080
	s_addc_u32 s29, s27, -1
	s_cmpk_eq_i32 s59, 0x54
	s_cselect_b32 s31, s1, s29
	s_cselect_b32 s30, s0, s28
	s_cselect_b32 s29, s25, s58
	s_cselect_b32 s28, s24, s57
	v_lshl_add_u64 v[146:147], s[26:27], 0, v[138:139]
	s_add_i32 m0, s39, 0xc000
	global_load_lds_dwordx4 v[146:147], off
	v_lshl_add_u64 v[146:147], s[26:27], 0, v[140:141]
	s_add_i32 m0, s39, 0xe000
	s_nop 0
	global_load_lds_dwordx4 v[146:147], off
	s_cmp_lg_u32 s100, 0
	s_cbranch_scc1 .Lrx_1562_0
	s_waitcnt vmcnt(8)

.LBB0_1694:
	v_readlane_b32 s38, v254, 1
	v_readlane_b32 s39, v254, 2
	s_mov_b32 s35, s99
	s_add_i32 s57, s57, 1
	s_mul_i32 s10, s57, s63
	s_waitcnt lgkmcnt(0)
	ds_read_b128 v[156:159], v176
	ds_read_b128 v[160:163], v176 offset:1024
	ds_read_b128 v[164:167], v176 offset:2048
	ds_read_b128 v[168:171], v176 offset:3072
	ds_read_b128 v[180:183], v177
	ds_read_b128 v[184:187], v177 offset:1024
	ds_read_b128 v[188:191], v177 offset:2048
	ds_read_b128 v[192:195], v177 offset:3072
	ds_read_b128 v[196:199], v178
	ds_read_b128 v[200:203], v178 offset:1024
	ds_read_b128 v[204:207], v178 offset:2048
	ds_read_b128 v[208:211], v178 offset:3072
	ds_read_b128 v[212:215], v178 offset:4096
	ds_read_b128 v[216:219], v178 offset:5120
	ds_read_b128 v[220:223], v178 offset:6144
	ds_read_b128 v[224:227], v178 offset:7168
	s_mul_hi_u32 s11, s57, s35
	s_add_i32 s11, s11, s10
	s_mul_i32 s10, s57, s35
	v_readlane_b32 s35, v254, 14
	s_add_u32 s38, s10, s35
	s_addc_u32 s39, s11, s64
	v_cmp_gt_i64_e32 vcc, s[38:39], v[154:155]
	v_cmp_lt_i64_e64 s[10:11], s[38:39], v[152:153]
	s_cbranch_vccnz .LBB0_1696
	s_ashr_i32 s34, s38, 31
	s_lshr_b32 s34, s34, 29
	s_add_i32 s34, s38, s34
	s_ashr_i32 s35, s34, 3
	s_and_b32 s34, s34, -8
	s_sub_i32 s34, s38, s34
	s_cmp_lt_i32 s34, 0
	s_movk_i32 s36, 0x191
	s_cselect_b32 s36, s36, 0x190
	s_mul_i32 s34, s34, s36
	s_add_i32 s34, s34, s35
	s_mul_hi_i32 s35, s34, 0x51eb851f
	s_lshr_b32 s36, s35, 31
	s_ashr_i32 s35, s35, 6
	s_add_i32 s35, s35, s36
	s_lshl_b32 s36, s35, 3
	s_sub_i32 s37, 0x80, s36
	s_min_i32 s37, s37, 8
	s_abs_i32 s38, s37
	v_cvt_f32_u32_e32 v2, s38
	s_sub_i32 s40, 0, s38
	s_mulk_i32 s35, 0xc8
	s_sub_i32 s35, s34, s35
	v_rcp_iflag_f32_e32 v2, v2
	s_abs_i32 s34, s35
	s_xor_b32 s39, s35, s37
	s_ashr_i32 s39, s39, 31
	v_mul_f32_e32 v2, 0x4f7ffffe, v2
	v_cvt_u32_f32_e32 v2, v2
	s_nop 0
	v_readfirstlane_b32 s41, v2
	s_mul_i32 s40, s40, s41
	s_mul_hi_u32 s40, s41, s40
	s_add_i32 s41, s41, s40
	s_mul_hi_u32 s40, s34, s41
	s_mul_i32 s41, s40, s38
	s_sub_i32 s34, s34, s41
	s_add_i32 s43, s40, 1
	s_sub_i32 s41, s34, s38
	s_cmp_ge_u32 s34, s38
	s_cselect_b32 s40, s43, s40
	s_cselect_b32 s34, s41, s34
	s_add_i32 s41, s40, 1
	s_cmp_ge_u32 s34, s38
	s_cselect_b32 s34, s41, s40
	s_xor_b32 s34, s34, s39
	s_sub_i32 s34, s34, s39
	s_mul_i32 s37, s34, s37
	s_sub_i32 s35, s35, s37
	s_add_i32 s36, s36, s35
.LBB0_1696:
	s_ashr_i32 s37, s36, 31
	s_lshl_b64 s[38:39], s[36:37], 20
	s_add_u32 s38, s20, s38
	s_addc_u32 s39, s21, s39
	s_and_b64 s[40:41], s[10:11], exec
	s_cselect_b32 s37, s39, s47
	s_cselect_b32 s43, s38, s46
	s_ashr_i32 s35, s34, 31
	s_lshl_b64 s[40:41], s[34:35], 20
	s_add_u32 s40, s23, s40
	s_addc_u32 s41, s33, s41
	s_and_b64 s[50:51], s[10:11], exec
	s_cselect_b32 s35, s41, s49
	s_cselect_b32 s45, s40, s48
	s_lshl_b32 s50, s44, 8
	s_ashr_i32 s51, s50, 31
	v_lshl_add_u64 v[238:239], s[50:51], 2, v[140:141]
	global_load_dword v240, v[238:239], off
	global_load_dword v242, v[238:239], off offset:64
	global_load_dword v244, v[238:239], off offset:128
	global_load_dword v246, v[238:239], off offset:192
	global_load_dword v248, v[238:239], off offset:512
	global_load_dword v250, v[238:239], off offset:576
	global_load_dword v252, v[238:239], off offset:640
	global_load_dword v238, v[238:239], off offset:704
	s_add_u32 s46, s46, 0x80080
	s_addc_u32 s47, s47, 0
	s_add_u32 s69, s48, 0x100
	s_addc_u32 s70, s49, 0
	s_mov_b32 s71, -2
	s_waitcnt vmcnt(0)
	s_add_u32 s48, s46, 0xfff80080
	s_addc_u32 s49, s47, -1
	s_cmp_eq_u32 s71, 28
	s_cselect_b32 s51, s37, s49
	s_cselect_b32 s50, s43, s48
	s_cselect_b32 s49, s35, s70
	s_cselect_b32 s48, s45, s69
	v_lshl_add_u64 v[172:173], s[46:47], 0, v[148:149]
	s_add_i32 m0, s53, 0xc000
	global_load_lds_dwordx4 v[172:173], off
	v_lshl_add_u64 v[172:173], s[46:47], 0, v[150:151]
	s_add_i32 m0, s53, 0xe000
	s_nop 0
	global_load_lds_dwordx4 v[172:173], off
	s_waitcnt vmcnt(8)
	s_waitcnt lgkmcnt(0)
	s_setprio 1
	s_barrier
	v_mfma_f32_16x16x32_bf16 v[126:129], v[156:159], v[196:199], 0
	v_mfma_f32_16x16x32_bf16 v[122:125], v[164:167], v[196:199], 0
	v_mfma_f32_16x16x32_bf16 v[118:121], v[156:159], v[204:207], 0
	v_mfma_f32_16x16x32_bf16 v[114:117], v[164:167], v[204:207], 0
	v_mfma_f32_16x16x32_bf16 v[110:113], v[156:159], v[212:215], 0
	v_mfma_f32_16x16x32_bf16 v[106:109], v[164:167], v[212:215], 0
	v_mfma_f32_16x16x32_bf16 v[102:105], v[156:159], v[220:223], 0
	v_mfma_f32_16x16x32_bf16 v[98:101], v[164:167], v[220:223], 0
	v_mfma_f32_16x16x32_bf16 v[126:129], v[160:163], v[200:203], v[126:129]
	v_mfma_f32_16x16x32_bf16 v[122:125], v[168:171], v[200:203], v[122:125]
	v_mfma_f32_16x16x32_bf16 v[118:121], v[160:163], v[208:211], v[118:121]
	v_mfma_f32_16x16x32_bf16 v[114:117], v[168:171], v[208:211], v[114:117]
	v_mfma_f32_16x16x32_bf16 v[110:113], v[160:163], v[216:219], v[110:113]
	v_mfma_f32_16x16x32_bf16 v[106:109], v[168:171], v[216:219], v[106:109]
	v_mfma_f32_16x16x32_bf16 v[102:105], v[160:163], v[224:227], v[102:105]
	v_mfma_f32_16x16x32_bf16 v[98:101], v[168:171], v[224:227], v[98:101]
	s_setprio 0
	s_setprio 1
	v_mfma_f32_16x16x32_bf16 v[38:41], v[180:183], v[196:199], 0
	v_mfma_f32_16x16x32_bf16 v[34:37], v[188:191], v[196:199], 0
	v_mfma_f32_16x16x32_bf16 v[46:49], v[180:183], v[204:207], 0
	v_mfma_f32_16x16x32_bf16 v[42:45], v[188:191], v[204:207], 0
	v_mfma_f32_16x16x32_bf16 v[54:57], v[180:183], v[212:215], 0
	v_mfma_f32_16x16x32_bf16 v[50:53], v[188:191], v[212:215], 0
	v_mfma_f32_16x16x32_bf16 v[62:65], v[180:183], v[220:223], 0
	v_mfma_f32_16x16x32_bf16 v[58:61], v[188:191], v[220:223], 0
	v_mfma_f32_16x16x32_bf16 v[38:41], v[184:187], v[200:203], v[38:41]
	v_mfma_f32_16x16x32_bf16 v[34:37], v[192:195], v[200:203], v[34:37]
	v_mfma_f32_16x16x32_bf16 v[46:49], v[184:187], v[208:211], v[46:49]
	v_mfma_f32_16x16x32_bf16 v[42:45], v[192:195], v[208:211], v[42:45]
	v_mfma_f32_16x16x32_bf16 v[54:57], v[184:187], v[216:219], v[54:57]
	v_mfma_f32_16x16x32_bf16 v[50:53], v[192:195], v[216:219], v[50:53]
	v_mfma_f32_16x16x32_bf16 v[62:65], v[184:187], v[224:227], v[62:65]
	v_mfma_f32_16x16x32_bf16 v[58:61], v[192:195], v[224:227], v[58:61]
	s_barrier
	s_setprio 0
	s_add_i32 s72, s65, s52
	v_lshl_add_u64 v[172:173], s[48:49], 0, v[132:133]
	s_mov_b32 m0, s72
	ds_read_b128 v[196:199], v178 offset:16384
	ds_read_b128 v[200:203], v178 offset:17408
	ds_read_b128 v[204:207], v178 offset:18432
	ds_read_b128 v[208:211], v178 offset:19456
	ds_read_b128 v[212:215], v178 offset:20480
	ds_read_b128 v[216:219], v178 offset:21504
	ds_read_b128 v[220:223], v178 offset:22528
	ds_read_b128 v[224:227], v178 offset:23552
	global_load_lds_dwordx4 v[172:173], off
	s_add_i32 m0, s72, 0x2000
	s_add_u32 s72, s48, 0x80000
	v_lshl_add_u64 v[228:229], s[48:49], 0, v[136:137]
	s_addc_u32 s73, s49, 0
	s_add_i32 s74, s66, s52
	global_load_lds_dwordx4 v[228:229], off
	v_lshl_add_u64 v[230:231], s[72:73], 0, v[132:133]
	s_mov_b32 m0, s74
	v_lshl_add_u64 v[232:233], s[50:51], 0, v[134:135]
	global_load_lds_dwordx4 v[230:231], off
	v_lshl_add_u64 v[230:231], s[72:73], 0, v[136:137]
	s_add_i32 m0, s74, 0x2000
	s_nop 0
	global_load_lds_dwordx4 v[230:231], off
	v_lshl_add_u64 v[230:231], s[50:51], 0, v[130:131]
	s_mov_b32 m0, s53
	s_nop 0
	global_load_lds_dwordx4 v[230:231], off
	s_mov_b32 m0, s54
	s_nop 0
	global_load_lds_dwordx4 v[232:233], off
	s_waitcnt vmcnt(8)
	s_waitcnt lgkmcnt(0)
	s_setprio 1
	s_barrier
	v_mfma_f32_16x16x32_bf16 v[94:97], v[156:159], v[196:199], 0
	v_mfma_f32_16x16x32_bf16 v[90:93], v[164:167], v[196:199], 0
	v_mfma_f32_16x16x32_bf16 v[86:89], v[156:159], v[204:207], 0
	v_mfma_f32_16x16x32_bf16 v[82:85], v[164:167], v[204:207], 0
	v_mfma_f32_16x16x32_bf16 v[78:81], v[156:159], v[212:215], 0
	v_mfma_f32_16x16x32_bf16 v[74:77], v[164:167], v[212:215], 0
	v_mfma_f32_16x16x32_bf16 v[70:73], v[156:159], v[220:223], 0
	v_mfma_f32_16x16x32_bf16 v[66:69], v[164:167], v[220:223], 0
	v_mfma_f32_16x16x32_bf16 v[94:97], v[160:163], v[200:203], v[94:97]
	v_mfma_f32_16x16x32_bf16 v[90:93], v[168:171], v[200:203], v[90:93]
	v_mfma_f32_16x16x32_bf16 v[86:89], v[160:163], v[208:211], v[86:89]
	v_mfma_f32_16x16x32_bf16 v[82:85], v[168:171], v[208:211], v[82:85]
	v_mfma_f32_16x16x32_bf16 v[78:81], v[160:163], v[216:219], v[78:81]
	v_mfma_f32_16x16x32_bf16 v[74:77], v[168:171], v[216:219], v[74:77]
	v_mfma_f32_16x16x32_bf16 v[70:73], v[160:163], v[224:227], v[70:73]
	v_mfma_f32_16x16x32_bf16 v[66:69], v[168:171], v[224:227], v[66:69]
	s_setprio 0
	s_setprio 1
	v_mfma_f32_16x16x32_bf16 v[6:9], v[180:183], v[196:199], 0
	v_mfma_f32_16x16x32_bf16 v[2:5], v[188:191], v[196:199], 0
	v_mfma_f32_16x16x32_bf16 v[18:21], v[180:183], v[204:207], 0
	v_mfma_f32_16x16x32_bf16 v[14:17], v[188:191], v[204:207], 0
	v_mfma_f32_16x16x32_bf16 v[26:29], v[180:183], v[212:215], 0
	v_mfma_f32_16x16x32_bf16 v[22:25], v[188:191], v[212:215], 0
	v_mfma_f32_16x16x32_bf16 v[30:33], v[180:183], v[220:223], 0
	v_mfma_f32_16x16x32_bf16 v[10:13], v[188:191], v[220:223], 0
	v_mfma_f32_16x16x32_bf16 v[6:9], v[184:187], v[200:203], v[6:9]
	v_mfma_f32_16x16x32_bf16 v[2:5], v[192:195], v[200:203], v[2:5]
	v_mfma_f32_16x16x32_bf16 v[18:21], v[184:187], v[208:211], v[18:21]
	v_mfma_f32_16x16x32_bf16 v[14:17], v[192:195], v[208:211], v[14:17]
	v_mfma_f32_16x16x32_bf16 v[26:29], v[184:187], v[216:219], v[26:29]
	v_mfma_f32_16x16x32_bf16 v[22:25], v[192:195], v[216:219], v[22:25]
	v_mfma_f32_16x16x32_bf16 v[30:33], v[184:187], v[224:227], v[30:33]
	v_mfma_f32_16x16x32_bf16 v[10:13], v[192:195], v[224:227], v[10:13]
	s_barrier
	s_setprio 0
	s_add_i32 s72, 0, 0x18000
	v_add_u32_e32 v138, s72, v174
	s_add_i32 s73, 0, 0x1c000
	ds_read_b128 v[156:159], v138
	ds_read_b128 v[160:163], v138 offset:1024
	ds_read_b128 v[164:167], v138 offset:2048
	ds_read_b128 v[168:171], v138 offset:3072
	v_add_u32_e32 v138, s73, v174
	ds_read_b128 v[180:183], v138
	ds_read_b128 v[184:187], v138 offset:1024
	ds_read_b128 v[188:191], v138 offset:2048
	ds_read_b128 v[192:195], v138 offset:3072
	s_add_u32 s50, s50, 0x80000
	s_addc_u32 s51, s51, 0
	s_mov_b32 m0, s55
	v_lshl_add_u64 v[234:235], s[50:51], 0, v[130:131]
	ds_read_b128 v[196:199], v178 offset:32768
	ds_read_b128 v[200:203], v178 offset:33792
	ds_read_b128 v[204:207], v178 offset:34816
	ds_read_b128 v[208:211], v178 offset:35840
	ds_read_b128 v[212:215], v178 offset:36864
	ds_read_b128 v[216:219], v178 offset:37888
	ds_read_b128 v[220:223], v178 offset:38912
	ds_read_b128 v[224:227], v178 offset:39936
	global_load_lds_dwordx4 v[234:235], off
	v_lshl_add_u64 v[234:235], s[50:51], 0, v[134:135]
	s_mov_b32 m0, s56
	s_nop 0
	global_load_lds_dwordx4 v[234:235], off
	s_waitcnt vmcnt(8)
	s_waitcnt lgkmcnt(0)
	s_setprio 1
	s_barrier
	v_mfma_f32_16x16x32_bf16 v[126:129], v[156:159], v[196:199], v[126:129]
	v_mfma_f32_16x16x32_bf16 v[122:125], v[164:167], v[196:199], v[122:125]
	v_mfma_f32_16x16x32_bf16 v[118:121], v[156:159], v[204:207], v[118:121]
	v_mfma_f32_16x16x32_bf16 v[114:117], v[164:167], v[204:207], v[114:117]
	v_mfma_f32_16x16x32_bf16 v[110:113], v[156:159], v[212:215], v[110:113]
	v_mfma_f32_16x16x32_bf16 v[106:109], v[164:167], v[212:215], v[106:109]
	v_mfma_f32_16x16x32_bf16 v[102:105], v[156:159], v[220:223], v[102:105]
	v_mfma_f32_16x16x32_bf16 v[98:101], v[164:167], v[220:223], v[98:101]
	v_mfma_f32_16x16x32_bf16 v[126:129], v[160:163], v[200:203], v[126:129]
	v_mfma_f32_16x16x32_bf16 v[122:125], v[168:171], v[200:203], v[122:125]
	v_mfma_f32_16x16x32_bf16 v[118:121], v[160:163], v[208:211], v[118:121]
	v_mfma_f32_16x16x32_bf16 v[114:117], v[168:171], v[208:211], v[114:117]
	v_mfma_f32_16x16x32_bf16 v[110:113], v[160:163], v[216:219], v[110:113]
	v_mfma_f32_16x16x32_bf16 v[106:109], v[168:171], v[216:219], v[106:109]
	v_mfma_f32_16x16x32_bf16 v[102:105], v[160:163], v[224:227], v[102:105]
	v_mfma_f32_16x16x32_bf16 v[98:101], v[168:171], v[224:227], v[98:101]
	s_setprio 0
	s_setprio 1
	v_mfma_f32_16x16x32_bf16 v[38:41], v[180:183], v[196:199], v[38:41]
	v_mfma_f32_16x16x32_bf16 v[34:37], v[188:191], v[196:199], v[34:37]
	v_mfma_f32_16x16x32_bf16 v[46:49], v[180:183], v[204:207], v[46:49]
	v_mfma_f32_16x16x32_bf16 v[42:45], v[188:191], v[204:207], v[42:45]
	v_mfma_f32_16x16x32_bf16 v[54:57], v[180:183], v[212:215], v[54:57]
	v_mfma_f32_16x16x32_bf16 v[50:53], v[188:191], v[212:215], v[50:53]
	v_mfma_f32_16x16x32_bf16 v[62:65], v[180:183], v[220:223], v[62:65]
	v_mfma_f32_16x16x32_bf16 v[58:61], v[188:191], v[220:223], v[58:61]
	v_mfma_f32_16x16x32_bf16 v[38:41], v[184:187], v[200:203], v[38:41]
	v_mfma_f32_16x16x32_bf16 v[34:37], v[192:195], v[200:203], v[34:37]
	v_mfma_f32_16x16x32_bf16 v[46:49], v[184:187], v[208:211], v[46:49]
	v_mfma_f32_16x16x32_bf16 v[42:45], v[192:195], v[208:211], v[42:45]
	v_mfma_f32_16x16x32_bf16 v[54:57], v[184:187], v[216:219], v[54:57]
	v_mfma_f32_16x16x32_bf16 v[50:53], v[192:195], v[216:219], v[50:53]
	v_mfma_f32_16x16x32_bf16 v[62:65], v[184:187], v[224:227], v[62:65]
	v_mfma_f32_16x16x32_bf16 v[58:61], v[192:195], v[224:227], v[58:61]
	s_barrier
	s_setprio 0
	s_add_i32 s50, s72, s52
	v_lshl_add_u64 v[172:173], v[172:173], 0, s[6:7]
	s_mov_b32 m0, s50
	ds_read_b128 v[196:199], v178 offset:49152
	ds_read_b128 v[200:203], v178 offset:50176
	ds_read_b128 v[204:207], v178 offset:51200
	ds_read_b128 v[208:211], v178 offset:52224
	ds_read_b128 v[212:215], v178 offset:53248
	ds_read_b128 v[216:219], v178 offset:54272
	ds_read_b128 v[220:223], v178 offset:55296
	ds_read_b128 v[224:227], v178 offset:56320
	global_load_lds_dwordx4 v[172:173], off
	s_add_i32 m0, s50, 0x2000
	s_add_u32 s48, s48, 0x80080
	v_lshl_add_u64 v[172:173], v[228:229], 0, s[6:7]
	s_addc_u32 s49, s49, 0
	s_add_i32 s50, s73, s52
	global_load_lds_dwordx4 v[172:173], off
	v_lshl_add_u64 v[172:173], s[48:49], 0, v[132:133]
	s_mov_b32 m0, s50
	s_nop 0
	global_load_lds_dwordx4 v[172:173], off
	v_lshl_add_u64 v[172:173], s[48:49], 0, v[136:137]
	s_add_i32 m0, s50, 0x2000
	s_nop 0
	global_load_lds_dwordx4 v[172:173], off
	v_lshl_add_u64 v[172:173], v[230:231], 0, s[6:7]
	s_mov_b32 m0, s61
	s_nop 0
	global_load_lds_dwordx4 v[172:173], off
	v_lshl_add_u64 v[172:173], v[232:233], 0, s[6:7]
	s_mov_b32 m0, s62
	s_nop 0
	global_load_lds_dwordx4 v[172:173], off
	s_waitcnt vmcnt(8)
	s_waitcnt lgkmcnt(0)
	s_setprio 1
	s_barrier
	v_mfma_f32_16x16x32_bf16 v[94:97], v[156:159], v[196:199], v[94:97]
	v_mfma_f32_16x16x32_bf16 v[90:93], v[164:167], v[196:199], v[90:93]
	v_mfma_f32_16x16x32_bf16 v[86:89], v[156:159], v[204:207], v[86:89]
	v_mfma_f32_16x16x32_bf16 v[82:85], v[164:167], v[204:207], v[82:85]
	v_mfma_f32_16x16x32_bf16 v[78:81], v[156:159], v[212:215], v[78:81]
	v_mfma_f32_16x16x32_bf16 v[74:77], v[164:167], v[212:215], v[74:77]
	v_mfma_f32_16x16x32_bf16 v[70:73], v[156:159], v[220:223], v[70:73]
	v_mfma_f32_16x16x32_bf16 v[66:69], v[164:167], v[220:223], v[66:69]
	v_mfma_f32_16x16x32_bf16 v[94:97], v[160:163], v[200:203], v[94:97]
	v_mfma_f32_16x16x32_bf16 v[90:93], v[168:171], v[200:203], v[90:93]
	v_mfma_f32_16x16x32_bf16 v[86:89], v[160:163], v[208:211], v[86:89]
	v_mfma_f32_16x16x32_bf16 v[82:85], v[168:171], v[208:211], v[82:85]
	v_mfma_f32_16x16x32_bf16 v[78:81], v[160:163], v[216:219], v[78:81]
	v_mfma_f32_16x16x32_bf16 v[74:77], v[168:171], v[216:219], v[74:77]
	v_mfma_f32_16x16x32_bf16 v[70:73], v[160:163], v[224:227], v[70:73]
	v_mfma_f32_16x16x32_bf16 v[66:69], v[168:171], v[224:227], v[66:69]
	s_setprio 0
	s_setprio 1
	v_mfma_f32_16x16x32_bf16 v[6:9], v[180:183], v[196:199], v[6:9]
	v_mfma_f32_16x16x32_bf16 v[2:5], v[188:191], v[196:199], v[2:5]
	v_mfma_f32_16x16x32_bf16 v[18:21], v[180:183], v[204:207], v[18:21]
	v_mfma_f32_16x16x32_bf16 v[14:17], v[188:191], v[204:207], v[14:17]
	v_mfma_f32_16x16x32_bf16 v[26:29], v[180:183], v[212:215], v[26:29]
	v_mfma_f32_16x16x32_bf16 v[22:25], v[188:191], v[212:215], v[22:25]
	v_mfma_f32_16x16x32_bf16 v[30:33], v[180:183], v[220:223], v[30:33]
	v_mfma_f32_16x16x32_bf16 v[10:13], v[188:191], v[220:223], v[10:13]
	v_mfma_f32_16x16x32_bf16 v[6:9], v[184:187], v[200:203], v[6:9]
	v_mfma_f32_16x16x32_bf16 v[2:5], v[192:195], v[200:203], v[2:5]
	v_mfma_f32_16x16x32_bf16 v[18:21], v[184:187], v[208:211], v[18:21]
	v_mfma_f32_16x16x32_bf16 v[14:17], v[192:195], v[208:211], v[14:17]
	v_mfma_f32_16x16x32_bf16 v[26:29], v[184:187], v[216:219], v[26:29]
	v_mfma_f32_16x16x32_bf16 v[22:25], v[192:195], v[216:219], v[22:25]
	v_mfma_f32_16x16x32_bf16 v[30:33], v[184:187], v[224:227], v[30:33]
	v_mfma_f32_16x16x32_bf16 v[10:13], v[192:195], v[224:227], v[10:13]
	s_barrier
	s_setprio 0
	s_add_i32 s71, s71, 2
	s_add_u32 s46, s46, 0x100
	s_addc_u32 s47, s47, 0
	s_add_u32 s69, s69, 0x100
	s_addc_u32 s70, s70, 0
	s_cmp_gt_u32 s71, 29

.LBB0_2107:
	v_readlane_b32 s26, v254, 1
	v_readlane_b32 s27, v254, 2
	s_mov_b32 s23, s99
	s_add_i32 s46, s46, 1
	s_mul_i32 s4, s46, s49
	s_waitcnt lgkmcnt(0)
	ds_read_b128 v[154:157], v150
	ds_read_b128 v[158:161], v150 offset:1024
	ds_read_b128 v[162:165], v150 offset:2048
	ds_read_b128 v[166:169], v150 offset:3072
	ds_read_b128 v[170:173], v151
	ds_read_b128 v[174:177], v151 offset:1024
	ds_read_b128 v[178:181], v151 offset:2048
	ds_read_b128 v[182:185], v151 offset:3072
	ds_read_b128 v[186:189], v152
	ds_read_b128 v[190:193], v152 offset:1024
	ds_read_b128 v[194:197], v152 offset:2048
	ds_read_b128 v[198:201], v152 offset:3072
	ds_read_b128 v[202:205], v152 offset:4096
	ds_read_b128 v[206:209], v152 offset:5120
	ds_read_b128 v[210:213], v152 offset:6144
	ds_read_b128 v[214:217], v152 offset:7168
	s_mul_hi_u32 s5, s46, s23
	s_add_i32 s5, s5, s4
	s_mul_i32 s4, s46, s23
	v_readlane_b32 s23, v254, 14
	s_add_u32 s26, s4, s23
	s_addc_u32 s27, s5, s33
	v_cmp_gt_i64_e32 vcc, s[26:27], v[144:145]
	v_cmp_lt_i64_e64 s[4:5], s[26:27], v[142:143]
	s_cbranch_vccnz .LBB0_2113
	s_ashr_i32 s22, s26, 31
	s_lshr_b32 s22, s22, 29
	s_add_i32 s24, s26, s22
	s_and_b32 s22, s24, -8
	s_sub_i32 s25, s26, s22
	s_cmp_gt_i32 s25, -1
	s_mov_b64 s[22:23], -1
	s_cbranch_scc0 .LBB0_2110
	s_lshl_b32 s26, s25, 7
	s_mov_b64 s[22:23], 0

.LBB0_2113:
	s_ashr_i32 s25, s24, 31
	s_lshl_b64 s[26:27], s[24:25], 20
	v_readlane_b32 s28, v254, 22
	v_readlane_b32 s29, v254, 23
	s_add_u32 s26, s28, s26
	s_addc_u32 s27, s29, s27
	s_and_b64 s[28:29], s[4:5], exec
	s_cselect_b32 s25, s27, s35
	s_cselect_b32 s57, s26, s34
	s_ashr_i32 s23, s22, 31
	s_lshl_b64 s[28:29], s[22:23], 20
	s_add_u32 s28, s40, s28
	s_addc_u32 s29, s41, s29
	s_and_b64 s[38:39], s[4:5], exec
	s_cselect_b32 s23, s29, s37
	s_cselect_b32 s58, s28, s36
	s_add_u32 s34, s34, 0x80080
	s_addc_u32 s35, s35, 0
	s_add_u32 s59, s36, 0x100
	s_addc_u32 s60, s37, 0
	s_mov_b32 s61, -2
	s_add_u32 s36, s34, 0xfff80080
	s_addc_u32 s37, s35, -1
	s_cmp_eq_u32 s61, 28
	s_cselect_b32 s39, s25, s37
	s_cselect_b32 s38, s57, s36
	s_cselect_b32 s37, s23, s60
	s_cselect_b32 s36, s58, s59
	v_lshl_add_u64 v[146:147], s[34:35], 0, v[138:139]
	s_add_i32 m0, s31, 0xc000
	global_load_lds_dwordx4 v[146:147], off
	v_lshl_add_u64 v[146:147], s[34:35], 0, v[140:141]
	s_add_i32 m0, s31, 0xe000
	s_nop 0
	global_load_lds_dwordx4 v[146:147], off
	s_cmp_lg_u32 s100, 0
	s_cbranch_scc1 .Lrx_2114_0
	s_waitcnt vmcnt(8)

.LBB0_2363:
	v_readlane_b32 s26, v254, 1
	v_readlane_b32 s27, v254, 2
	s_mov_b32 s23, s99
	s_add_i32 s7, s7, 1
	s_mul_i32 s4, s7, s59
	s_waitcnt lgkmcnt(0)
	ds_read_b128 v[18:21], v186
	ds_read_b128 v[22:25], v186 offset:1024
	ds_read_b128 v[26:29], v186 offset:2048
	ds_read_b128 v[30:33], v186 offset:3072
	ds_read_b128 v[2:5], v187
	ds_read_b128 v[6:9], v187 offset:1024
	ds_read_b128 v[10:13], v187 offset:2048
	ds_read_b128 v[14:17], v187 offset:3072
	ds_read_b128 v[176:179], v188
	ds_read_b128 v[180:183], v188 offset:1024
	ds_read_b128 v[192:195], v188 offset:2048
	ds_read_b128 v[196:199], v188 offset:3072
	ds_read_b128 v[200:203], v188 offset:4096
	ds_read_b128 v[204:207], v188 offset:5120
	ds_read_b128 v[216:219], v188 offset:6144
	ds_read_b128 v[220:223], v188 offset:7168
	s_mul_hi_u32 s5, s7, s23
	s_add_i32 s5, s5, s4
	s_mul_i32 s4, s7, s23
	v_readlane_b32 s23, v254, 14
	s_add_u32 s26, s4, s23
	s_addc_u32 s27, s5, s45
	v_cmp_ge_i64_e32 vcc, s[26:27], v[174:175]
	v_cmp_lt_i64_e64 s[4:5], s[26:27], v[174:175]
	s_cbranch_vccnz .LBB0_2365
	s_ashr_i32 s22, s26, 31
	s_lshr_b32 s22, s22, 29
	s_add_i32 s22, s26, s22
	s_ashr_i32 s23, s22, 3
	s_and_b32 s22, s22, -8
	s_sub_i32 s22, s26, s22
	s_cmp_lt_i32 s22, 0
	s_cselect_b32 s24, s46, s44
	s_mul_i32 s22, s24, s22
	s_add_i32 s22, s22, s23
	s_mul_hi_i32 s23, s22, 0x92492493
	s_add_i32 s23, s23, s22
	s_lshr_b32 s24, s23, 31
	s_ashr_i32 s23, s23, 8
	s_add_i32 s23, s23, s24
	s_lshl_b32 s24, s23, 3
	s_sub_i32 s25, s58, s24
	s_min_i32 s25, s25, 8
	s_abs_i32 s26, s25
	v_cvt_f32_u32_e32 v210, s26
	s_sub_i32 s28, 0, s26
	s_mulk_i32 s23, 0x1c0
	s_sub_i32 s22, s22, s23
	v_rcp_iflag_f32_e32 v210, v210
	s_abs_i32 s23, s22
	s_xor_b32 s27, s22, s25
	s_ashr_i32 s27, s27, 31
	v_mul_f32_e32 v210, 0x4f7ffffe, v210
	v_cvt_u32_f32_e32 v210, v210
	s_nop 0
	v_readfirstlane_b32 s29, v210
	s_mul_i32 s28, s28, s29
	s_mul_hi_u32 s28, s29, s28
	s_add_i32 s29, s29, s28
	s_mul_hi_u32 s28, s23, s29
	s_mul_i32 s29, s28, s26
	s_sub_i32 s23, s23, s29
	s_add_i32 s38, s28, 1
	s_sub_i32 s29, s23, s26
	s_cmp_ge_u32 s23, s26
	s_cselect_b32 s28, s38, s28
	s_cselect_b32 s23, s29, s23
	s_add_i32 s29, s28, 1
	s_cmp_ge_u32 s23, s26
	s_cselect_b32 s23, s29, s28
	s_xor_b32 s23, s23, s27
	s_sub_i32 s64, s23, s27
	s_mul_i32 s23, s64, s25
	s_sub_i32 s22, s22, s23
	s_add_i32 s22, s22, s24
	s_cmp_ge_i32 s22, s57
	s_cselect_b64 s[24:25], -1, 0
	s_cmp_ge_i32 s22, s33
	v_cndmask_b32_e64 v210, 0, 1, s[24:25]
	s_cselect_b64 s[24:25], -1, 0
	s_cmp_ge_i32 s22, s52
	v_cndmask_b32_e64 v211, 0, 1, s[24:25]
	s_cselect_b64 s[24:25], -1, 0
	v_readfirstlane_b32 s23, v211
	v_readfirstlane_b32 s26, v210
	s_cmp_lg_u64 s[24:25], 0
	s_addc_u32 s23, s23, s26
	s_cmp_ge_i32 s22, s53
	s_cselect_b64 s[24:25], -1, 0
	s_cmp_ge_i32 s22, s54
	v_cndmask_b32_e64 v210, 0, 1, s[24:25]
	s_cselect_b64 s[24:25], -1, 0
	v_readfirstlane_b32 s26, v210
	s_cmp_lg_u64 s[24:25], 0
	s_addc_u32 s23, s23, s26
	s_cmp_ge_i32 s22, s55
	s_cselect_b64 s[24:25], -1, 0
	s_cmp_ge_i32 s22, s56
	v_cndmask_b32_e64 v210, 0, 1, s[24:25]
	s_cselect_b64 s[24:25], -1, 0
	v_readfirstlane_b32 s26, v210
	s_cmp_lg_u64 s[24:25], 0
	s_addc_u32 s23, s23, s26
	s_mul_i32 s23, s23, 56
	s_add_i32 s24, s23, s64
.LBB0_2365:
	s_ashr_i32 s23, s22, 31
	s_lshl_b64 s[26:27], s[22:23], 19
	s_add_u32 s26, s19, s26
	s_addc_u32 s27, s40, s27
	s_and_b64 s[28:29], s[4:5], exec
	s_cselect_b32 s23, s27, s35
	s_cselect_b32 s66, s26, s34
	s_ashr_i32 s25, s24, 31
	s_lshl_b64 s[28:29], s[24:25], 19
	s_add_u32 s28, s41, s28
	s_addc_u32 s29, s42, s29
	s_and_b64 s[38:39], s[4:5], exec
	s_cselect_b32 s25, s29, s37
	s_cselect_b32 s67, s28, s36
	s_add_u32 s34, s34, 0x40080
	s_addc_u32 s35, s35, 0
	s_add_u32 s68, s36, 0x100
	s_addc_u32 s69, s37, 0
	s_mov_b32 s70, -2
	s_add_u32 s36, s34, 0xfffc0080
	s_addc_u32 s37, s35, -1
	s_cmp_eq_u32 s70, 12
	s_cselect_b32 s39, s23, s37
	s_cselect_b32 s38, s66, s36
	s_cselect_b32 s37, s25, s69
	s_cselect_b32 s36, s67, s68
	v_lshl_add_u64 v[208:209], s[34:35], 0, v[170:171]
	s_add_i32 m0, s31, 0xc000
	global_load_lds_dwordx4 v[208:209], off
	v_lshl_add_u64 v[208:209], s[34:35], 0, v[172:173]
	s_add_i32 m0, s31, 0xe000
	s_nop 0
	global_load_lds_dwordx4 v[208:209], off
	s_cmp_lg_u32 s100, 0
	s_cbranch_scc1 .Lrx_2366_0
	s_waitcnt vmcnt(8)
